# E6 plus gate/up SwiGLU epilogue: rinv-slot (ss) indices of padding rows clamped to the tile's last valid slot, so no never-written slot-table memory is read
# baseline (speedup 1.0000x reference)
.LBB0_762:
	s_add_u32 s6, s2, 0x26000000
	s_addc_u32 s7, s3, 0
	s_add_u32 s48, s2, 0x2000000
	s_mul_i32 s47, s44, 3
	s_addc_u32 s49, s3, 0
	v_mbcnt_lo_u32_b32 v8, -1, 0
	v_mbcnt_hi_u32_b32 v8, -1, v8
	s_cmp_lt_i32 s46, s47
	v_add_u32_e32 v0, s42, v8
	s_cselect_b64 s[8:9], -1, 0
	s_cmp_ge_i32 s46, s47
	v_readfirstlane_b32 s20, v0
	s_cbranch_scc1 .LBB0_764
	s_mul_hi_i32 s12, s46, 0x55555556
	s_lshr_b32 s13, s12, 31
	s_add_i32 s64, s12, s13
	s_lshl_b32 s12, s64, 2
	s_add_i32 s12, s12, 0
	s_add_i32 s12, s12, 0x20400
	v_mov_b32_e32 v1, s12
	ds_read_b32 v1, v1
	s_mul_i32 s12, s64, -3
	s_add_i32 s28, s12, s46
	s_mov_b64 s[30:31], s[6:7]
	s_waitcnt lgkmcnt(0)
	v_readfirstlane_b32 s12, v1
	s_ashr_i32 s13, s12, 16
	s_lshl_b32 s14, s13, 2
	s_add_i32 s14, s14, 0
	s_add_i32 s14, s14, 0x20a00
	v_mov_b32_e32 v1, s14
	ds_read_b32 v1, v1
	s_lshl_b32 s12, s12, 8
	s_and_b32 s12, s12, 0xffff00
	s_lshl_b32 s14, s13, 15
	s_add_i32 s65, s14, s12
	s_waitcnt lgkmcnt(0)
	v_readfirstlane_b32 s14, v1
	s_sub_i32 s12, s14, s12
	s_mul_hi_i32 s15, s13, 0x180000
	s_mul_i32 s13, s13, 0x180000
	s_min_i32 s14, s12, 0x100
	s_mov_b32 s80, s14
	s_add_u32 s16, s48, s13
	s_addc_u32 s15, s49, s15
	s_ashr_i32 s29, s28, 31
	s_lshl_b64 s[12:13], s[28:29], 19
	s_add_u32 s36, s16, s12
	s_addc_u32 s37, s15, s13
	s_andn2_b64 vcc, exec, s[8:9]
	s_cbranch_vccz .LBB0_765
	s_branch .LBB0_798

.LBB0_777:
	s_andn2_b64 vcc, exec, s[2:3]
	s_mov_b32 s80, s63
	v_mov_b32_e32 v140, v158
	v_mov_b32_e32 v134, v155
	v_mov_b32_e32 v136, v156
	v_mov_b32_e32 v138, v157
	s_mov_b32 s65, s62
	s_mov_b32 s28, s22
	s_mov_b32 s64, s61
	s_mov_b64 s[36:37], s[24:25]
	s_mov_b64 s[30:31], s[26:27]
	s_cbranch_vccz .LBB0_797

.LBB0_794:
	s_add_i32 s81, s65, s80
	s_add_i32 s81, s81, -1
	v_add_u32_e32 v140, s65, v137
	v_min_i32_e32 v140, s81, v140
	v_ashrrev_i32_e32 v141, 31, v140
	v_lshl_add_u64 v[134:135], v[140:141], 2, s[16:17]
	global_load_dword v142, v[134:135], off
	v_mov_b32_e32 v162, v120
	v_add_u32_e32 v120, 16, v140
	v_mov_b32_e32 v163, v112
	v_mov_b32_e32 v112, v121
	v_min_i32_e32 v120, s81, v120
	v_ashrrev_i32_e32 v121, 31, v120
	v_lshl_add_u64 v[120:121], v[120:121], 2, s[16:17]
	global_load_dword v174, v[120:121], off
	v_mov_b32_e32 v160, v124
	v_mov_b32_e32 v164, v126
	v_mov_b32_e32 v166, v122
	v_add_u32_e32 v122, 32, v140
	v_add_u32_e32 v124, 48, v140
	v_add_u32_e32 v126, 0x80, v140
	v_mov_b32_e32 v161, v116
	v_mov_b32_e32 v116, v125
	v_mov_b32_e32 v165, v118
	v_mov_b32_e32 v167, v114
	v_mov_b32_e32 v118, v127
	v_mov_b32_e32 v114, v123
	v_add_u32_e32 v168, 0x90, v140
	v_add_u32_e32 v170, 0xa0, v140
	v_add_u32_e32 v140, 0xb0, v140
	v_min_i32_e32 v122, s81, v122
	v_ashrrev_i32_e32 v123, 31, v122
	v_min_i32_e32 v124, s81, v124
	v_ashrrev_i32_e32 v125, 31, v124
	v_min_i32_e32 v126, s81, v126
	v_ashrrev_i32_e32 v127, 31, v126
	v_min_i32_e32 v168, s81, v168
	v_ashrrev_i32_e32 v169, 31, v168
	v_min_i32_e32 v170, s81, v170
	v_ashrrev_i32_e32 v171, 31, v170
	v_min_i32_e32 v140, s81, v140
	v_ashrrev_i32_e32 v141, 31, v140
	v_lshl_add_u64 v[120:121], v[122:123], 2, s[16:17]
	v_lshl_add_u64 v[122:123], v[124:125], 2, s[16:17]
	v_lshl_add_u64 v[124:125], v[126:127], 2, s[16:17]
	v_lshl_add_u64 v[168:169], v[168:169], 2, s[16:17]
	v_lshl_add_u64 v[170:171], v[170:171], 2, s[16:17]
	v_lshl_add_u64 v[140:141], v[140:141], 2, s[16:17]
	global_load_dword v136, v[120:121], off
	global_load_dword v132, v[122:123], off
	global_load_dword v126, v[124:125], off
	s_nop 0
	global_load_dword v124, v[168:169], off
	global_load_dword v122, v[170:171], off
	global_load_dword v120, v[140:141], off
	v_lshl_or_b32 v144, s28, 7, v151
	v_lshl_add_u32 v138, s64, 8, v137
	v_mov_b64_e32 v[134:135], s[14:15]
	v_ashrrev_i32_e32 v145, 31, v144
	v_mad_i64_i32 v[172:173], s[30:31], v138, s59, v[134:135]
	s_and_b64 vcc, exec, s[2:3]
	s_mov_b64 s[2:3], -1
	s_waitcnt vmcnt(0)
	v_pk_mul_f32 v[116:117], v[116:117], v[142:143] op_sel_hi:[1,0]
	v_pk_mul_f32 v[112:113], v[112:113], v[142:143] op_sel_hi:[1,0]
	v_mul_f32_e32 v125, 0xbfb8aa3b, v117
	v_mul_f32_e32 v127, 0xbfb8aa3b, v113
	v_exp_f32_e32 v125, v125
	v_exp_f32_e32 v127, v127
	v_pk_mul_f32 v[140:141], v[160:161], v[142:143] op_sel_hi:[1,0]
	v_pk_mul_f32 v[160:161], v[162:163], v[142:143] op_sel_hi:[1,0]
	v_pk_mul_f32 v[162:163], v[164:165], v[142:143] op_sel_hi:[1,0]
	v_pk_mul_f32 v[164:165], v[166:167], v[142:143] op_sel_hi:[1,0]
	v_pk_mul_f32 v[118:119], v[118:119], v[142:143] op_sel_hi:[1,0]
	v_pk_mul_f32 v[114:115], v[114:115], v[142:143] op_sel_hi:[1,0]
	v_mul_f32_e32 v121, 0xbfb8aa3b, v141
	v_mul_f32_e32 v143, 0xbfb8aa3b, v165
	v_add_f32_e32 v125, 1.0, v125
	v_add_f32_e32 v127, 1.0, v127
	v_mul_f32_e32 v159, 0xbfb8aa3b, v119
	v_exp_f32_e32 v121, v121
	v_exp_f32_e32 v143, v143
	v_rcp_f32_e32 v125, v125
	v_rcp_f32_e32 v127, v127
	v_mul_f32_e32 v166, 0xbfb8aa3b, v115
	v_exp_f32_e32 v159, v159
	v_mul_f32_e32 v142, 0xbfb8aa3b, v163
	v_exp_f32_e32 v166, v166
	v_mul_f32_e32 v123, 0xbfb8aa3b, v161
	v_exp_f32_e32 v142, v142
	v_exp_f32_e32 v123, v123
	v_add_f32_e32 v121, 1.0, v121
	v_add_f32_e32 v143, 1.0, v143
	v_mul_f32_e32 v117, v117, v125
	v_mul_f32_e32 v113, v113, v127
	v_rcp_f32_e32 v121, v121
	v_rcp_f32_e32 v143, v143
	v_mul_f32_e32 v116, v116, v117
	v_mul_f32_e32 v117, v112, v113
	v_add_f32_e32 v113, 1.0, v159
	v_rcp_f32_e32 v113, v113
	v_add_f32_e32 v127, 1.0, v166
	v_add_f32_e32 v142, 1.0, v142
	v_rcp_f32_e32 v127, v127
	v_add_f32_e32 v123, 1.0, v123
	v_rcp_f32_e32 v142, v142
	v_rcp_f32_e32 v123, v123
	v_mul_f32_e32 v121, v141, v121
	v_mul_f32_e32 v112, v165, v143
	v_mul_f32_e32 v121, v140, v121
	v_mul_f32_e32 v140, v164, v112
	v_mul_f32_e32 v112, v119, v113
	v_mul_f32_e32 v141, v118, v112
	v_mul_f32_e32 v112, v115, v127
	v_mul_f32_e32 v125, v163, v142
	v_mul_f32_e32 v127, v114, v112
	v_lshlrev_b64 v[112:113], 1, v[144:145]
	v_mul_f32_e32 v123, v161, v123
	v_mul_f32_e32 v125, v162, v125
	v_lshl_add_u64 v[118:119], v[172:173], 0, v[112:113]
	v_cvt_pk_bf16_f32 v114, v121, v116
	v_cvt_pk_bf16_f32 v115, v125, v141
	v_mul_f32_e32 v123, v160, v123
	v_cvt_pk_bf16_f32 v116, v123, v117
	v_cvt_pk_bf16_f32 v117, v140, v127
	global_store_dwordx4 v[118:119], v[114:117], off
	s_nop 1
	v_mov_b32_e32 v114, v100
	v_mov_b32_e32 v115, v108
	v_pk_mul_f32 v[114:115], v[114:115], v[174:175] op_sel_hi:[1,0]
	v_mov_b32_e32 v116, v96
	v_mul_f32_e32 v100, 0xbfb8aa3b, v115
	v_mov_b32_e32 v117, v104
	v_exp_f32_e32 v100, v100
	v_pk_mul_f32 v[116:117], v[116:117], v[174:175] op_sel_hi:[1,0]
	v_mov_b32_e32 v108, v101
	v_mul_f32_e32 v96, 0xbfb8aa3b, v117
	v_exp_f32_e32 v96, v96
	v_add_f32_e32 v100, 1.0, v100
	v_rcp_f32_e32 v100, v100
	v_or_b32_e32 v104, 16, v138
	v_add_f32_e32 v96, 1.0, v96
	v_rcp_f32_e32 v96, v96
	v_mul_f32_e32 v100, v115, v100
	v_mul_f32_e32 v114, v114, v100
	v_pk_mul_f32 v[100:101], v[108:109], v[174:175] op_sel_hi:[1,0]
	v_mad_i64_i32 v[118:119], s[30:31], v104, s59, v[134:135]
	v_mul_f32_e32 v115, v117, v96
	v_mul_f32_e32 v96, 0xbfb8aa3b, v101
	v_mov_b32_e32 v104, v97
	v_exp_f32_e32 v108, v96
	v_pk_mul_f32 v[96:97], v[104:105], v[174:175] op_sel_hi:[1,0]
	v_mul_f32_e32 v109, v116, v115
	v_mul_f32_e32 v104, 0xbfb8aa3b, v97
	v_exp_f32_e32 v104, v104
	v_add_f32_e32 v105, 1.0, v108
	v_rcp_f32_e32 v108, v105
	v_mov_b32_e32 v105, v110
	v_add_f32_e32 v104, 1.0, v104
	v_rcp_f32_e32 v115, v104
	v_mov_b32_e32 v104, v102
	v_pk_mul_f32 v[104:105], v[104:105], v[174:175] op_sel_hi:[1,0]
	v_mul_f32_e32 v101, v101, v108
	v_mul_f32_e32 v102, 0xbfb8aa3b, v105
	v_exp_f32_e32 v102, v102
	v_mul_f32_e32 v108, v100, v101
	v_mov_b32_e32 v101, v106
	v_mul_f32_e32 v97, v97, v115
	v_add_f32_e32 v100, 1.0, v102
	v_rcp_f32_e32 v102, v100
	v_mov_b32_e32 v100, v98
	v_pk_mul_f32 v[100:101], v[100:101], v[174:175] op_sel_hi:[1,0]
	v_mul_f32_e32 v115, v96, v97
	v_mul_f32_e32 v98, 0xbfb8aa3b, v101
	v_exp_f32_e32 v98, v98
	v_mul_f32_e32 v96, v105, v102
	v_mul_f32_e32 v102, v104, v96
	v_mov_b32_e32 v110, v103
	v_add_f32_e32 v96, 1.0, v98
	v_rcp_f32_e32 v104, v96
	v_pk_mul_f32 v[96:97], v[110:111], v[174:175] op_sel_hi:[1,0]
	v_mov_b32_e32 v106, v99
	v_mul_f32_e32 v98, 0xbfb8aa3b, v97
	v_exp_f32_e32 v103, v98
	v_pk_mul_f32 v[98:99], v[106:107], v[174:175] op_sel_hi:[1,0]
	v_mul_f32_e32 v101, v101, v104
	v_mul_f32_e32 v105, 0xbfb8aa3b, v99
	v_exp_f32_e32 v105, v105
	v_add_f32_e32 v103, 1.0, v103
	v_rcp_f32_e32 v103, v103
	v_add_f32_e32 v104, 1.0, v105
	v_rcp_f32_e32 v104, v104
	v_mul_f32_e32 v97, v97, v103
	v_mul_f32_e32 v97, v96, v97
	v_mul_f32_e32 v105, v100, v101
	v_mul_f32_e32 v96, v99, v104
	v_mul_f32_e32 v99, v98, v96
	v_lshl_add_u64 v[100:101], v[118:119], 0, v[112:113]
	v_cvt_pk_bf16_f32 v96, v114, v108
	v_cvt_pk_bf16_f32 v97, v102, v97
	v_cvt_pk_bf16_f32 v98, v109, v115
	v_cvt_pk_bf16_f32 v99, v105, v99
	global_store_dwordx4 v[100:101], v[96:99], off
	s_nop 1
	v_mov_b32_e32 v96, v84
	v_mov_b32_e32 v97, v92
	v_pk_mul_f32 v[96:97], v[96:97], v[136:137] op_sel_hi:[1,0]
	v_mov_b32_e32 v98, v80
	v_mul_f32_e32 v84, 0xbfb8aa3b, v97
	v_mov_b32_e32 v99, v88
	v_exp_f32_e32 v84, v84
	v_pk_mul_f32 v[98:99], v[98:99], v[136:137] op_sel_hi:[1,0]
	v_mov_b32_e32 v92, v85
	v_mul_f32_e32 v80, 0xbfb8aa3b, v99
	v_exp_f32_e32 v80, v80
	v_add_f32_e32 v84, 1.0, v84
	v_rcp_f32_e32 v84, v84
	v_or_b32_e32 v88, 32, v138
	v_add_f32_e32 v80, 1.0, v80
	v_rcp_f32_e32 v80, v80
	v_mul_f32_e32 v84, v97, v84
	v_mul_f32_e32 v96, v96, v84
	v_pk_mul_f32 v[84:85], v[92:93], v[136:137] op_sel_hi:[1,0]
	v_mad_i64_i32 v[100:101], s[30:31], v88, s59, v[134:135]
	v_mul_f32_e32 v97, v99, v80
	v_mul_f32_e32 v80, 0xbfb8aa3b, v85
	v_mov_b32_e32 v88, v81
	v_exp_f32_e32 v92, v80
	v_pk_mul_f32 v[80:81], v[88:89], v[136:137] op_sel_hi:[1,0]
	v_mul_f32_e32 v93, v98, v97
	v_mul_f32_e32 v88, 0xbfb8aa3b, v81
	v_exp_f32_e32 v88, v88
	v_add_f32_e32 v89, 1.0, v92
	v_rcp_f32_e32 v92, v89
	v_mov_b32_e32 v89, v94
	v_add_f32_e32 v88, 1.0, v88
	v_rcp_f32_e32 v97, v88
	v_mov_b32_e32 v88, v86
	v_pk_mul_f32 v[88:89], v[88:89], v[136:137] op_sel_hi:[1,0]
	v_mul_f32_e32 v85, v85, v92
	v_mul_f32_e32 v86, 0xbfb8aa3b, v89
	v_exp_f32_e32 v86, v86
	v_mul_f32_e32 v92, v84, v85
	v_mov_b32_e32 v85, v90
	v_mul_f32_e32 v81, v81, v97
	v_add_f32_e32 v84, 1.0, v86
	v_rcp_f32_e32 v86, v84
	v_mov_b32_e32 v84, v82
	v_pk_mul_f32 v[84:85], v[84:85], v[136:137] op_sel_hi:[1,0]
	v_mul_f32_e32 v97, v80, v81
	v_mul_f32_e32 v82, 0xbfb8aa3b, v85
	v_exp_f32_e32 v82, v82
	v_mul_f32_e32 v80, v89, v86
	v_mul_f32_e32 v86, v88, v80
	v_mov_b32_e32 v94, v87
	v_add_f32_e32 v80, 1.0, v82
	v_rcp_f32_e32 v88, v80
	v_pk_mul_f32 v[80:81], v[94:95], v[136:137] op_sel_hi:[1,0]
	v_mov_b32_e32 v90, v83
	v_mul_f32_e32 v82, 0xbfb8aa3b, v81
	v_exp_f32_e32 v87, v82
	v_pk_mul_f32 v[82:83], v[90:91], v[136:137] op_sel_hi:[1,0]
	v_mul_f32_e32 v85, v85, v88
	v_mul_f32_e32 v89, 0xbfb8aa3b, v83
	v_exp_f32_e32 v89, v89
	v_add_f32_e32 v87, 1.0, v87
	v_rcp_f32_e32 v87, v87
	v_add_f32_e32 v88, 1.0, v89
	v_rcp_f32_e32 v88, v88
	v_mul_f32_e32 v81, v81, v87
	v_mul_f32_e32 v81, v80, v81
	v_mul_f32_e32 v89, v84, v85
	v_mul_f32_e32 v80, v83, v88
	v_mul_f32_e32 v83, v82, v80
	v_lshl_add_u64 v[84:85], v[100:101], 0, v[112:113]
	v_cvt_pk_bf16_f32 v80, v96, v92
	v_cvt_pk_bf16_f32 v81, v86, v81
	v_cvt_pk_bf16_f32 v82, v93, v97
	v_cvt_pk_bf16_f32 v83, v89, v83
	global_store_dwordx4 v[84:85], v[80:83], off
	s_nop 1
	v_mov_b32_e32 v80, v68
	v_mov_b32_e32 v81, v76
	v_pk_mul_f32 v[80:81], v[80:81], v[132:133] op_sel_hi:[1,0]
	v_mov_b32_e32 v82, v64
	v_mul_f32_e32 v68, 0xbfb8aa3b, v81
	v_mov_b32_e32 v83, v72
	v_exp_f32_e32 v68, v68
	v_pk_mul_f32 v[82:83], v[82:83], v[132:133] op_sel_hi:[1,0]
	v_mov_b32_e32 v76, v69
	v_mul_f32_e32 v64, 0xbfb8aa3b, v83
	v_exp_f32_e32 v64, v64
	v_add_f32_e32 v68, 1.0, v68
	v_rcp_f32_e32 v68, v68
	v_or_b32_e32 v72, 48, v138
	v_add_f32_e32 v64, 1.0, v64
	v_rcp_f32_e32 v64, v64
	v_mul_f32_e32 v68, v81, v68
	v_mul_f32_e32 v80, v80, v68
	v_pk_mul_f32 v[68:69], v[76:77], v[132:133] op_sel_hi:[1,0]
	v_mad_i64_i32 v[84:85], s[30:31], v72, s59, v[134:135]
	v_mul_f32_e32 v81, v83, v64
	v_mul_f32_e32 v64, 0xbfb8aa3b, v69
	v_mov_b32_e32 v72, v65
	v_exp_f32_e32 v76, v64
	v_pk_mul_f32 v[64:65], v[72:73], v[132:133] op_sel_hi:[1,0]
	v_mul_f32_e32 v77, v82, v81
	v_mul_f32_e32 v72, 0xbfb8aa3b, v65
	v_exp_f32_e32 v72, v72
	v_add_f32_e32 v73, 1.0, v76
	v_rcp_f32_e32 v76, v73
	v_mov_b32_e32 v73, v78
	v_add_f32_e32 v72, 1.0, v72
	v_rcp_f32_e32 v81, v72
	v_mov_b32_e32 v72, v70
	v_pk_mul_f32 v[72:73], v[72:73], v[132:133] op_sel_hi:[1,0]
	v_mul_f32_e32 v69, v69, v76
	v_mul_f32_e32 v70, 0xbfb8aa3b, v73
	v_exp_f32_e32 v70, v70
	v_mul_f32_e32 v76, v68, v69
	v_mov_b32_e32 v69, v74
	v_mul_f32_e32 v65, v65, v81
	v_add_f32_e32 v68, 1.0, v70
	v_rcp_f32_e32 v70, v68
	v_mov_b32_e32 v68, v66
	v_pk_mul_f32 v[68:69], v[68:69], v[132:133] op_sel_hi:[1,0]
	v_mul_f32_e32 v81, v64, v65
	v_mul_f32_e32 v66, 0xbfb8aa3b, v69
	v_exp_f32_e32 v66, v66
	v_mul_f32_e32 v64, v73, v70
	v_mul_f32_e32 v70, v72, v64
	v_mov_b32_e32 v78, v71
	v_add_f32_e32 v64, 1.0, v66
	v_rcp_f32_e32 v72, v64
	v_pk_mul_f32 v[64:65], v[78:79], v[132:133] op_sel_hi:[1,0]
	v_mov_b32_e32 v74, v67
	v_mul_f32_e32 v66, 0xbfb8aa3b, v65
	v_exp_f32_e32 v71, v66
	v_pk_mul_f32 v[66:67], v[74:75], v[132:133] op_sel_hi:[1,0]
	v_mul_f32_e32 v69, v69, v72
	v_mul_f32_e32 v73, 0xbfb8aa3b, v67
	v_exp_f32_e32 v73, v73
	v_add_f32_e32 v71, 1.0, v71
	v_rcp_f32_e32 v71, v71
	v_add_f32_e32 v72, 1.0, v73
	v_rcp_f32_e32 v72, v72
	v_mul_f32_e32 v65, v65, v71
	v_mul_f32_e32 v65, v64, v65
	v_mul_f32_e32 v73, v68, v69
	v_mul_f32_e32 v64, v67, v72
	v_mul_f32_e32 v67, v66, v64
	v_lshl_add_u64 v[68:69], v[84:85], 0, v[112:113]
	v_cvt_pk_bf16_f32 v64, v80, v76
	v_cvt_pk_bf16_f32 v65, v70, v65
	v_cvt_pk_bf16_f32 v66, v77, v81
	v_cvt_pk_bf16_f32 v67, v73, v67
	global_store_dwordx4 v[68:69], v[64:67], off
	s_nop 1
	v_mov_b32_e32 v64, v52
	v_mov_b32_e32 v65, v60
	v_pk_mul_f32 v[64:65], v[64:65], v[126:127] op_sel_hi:[1,0]
	v_mov_b32_e32 v66, v48
	v_mul_f32_e32 v52, 0xbfb8aa3b, v65
	v_mov_b32_e32 v67, v56
	v_exp_f32_e32 v52, v52
	v_pk_mul_f32 v[66:67], v[66:67], v[126:127] op_sel_hi:[1,0]
	v_mov_b32_e32 v60, v53
	v_mul_f32_e32 v48, 0xbfb8aa3b, v67
	v_exp_f32_e32 v48, v48
	v_add_f32_e32 v52, 1.0, v52
	v_rcp_f32_e32 v52, v52
	v_add_u32_e32 v56, 0x80, v138
	v_add_f32_e32 v48, 1.0, v48
	v_rcp_f32_e32 v48, v48
	v_mul_f32_e32 v52, v65, v52
	v_mul_f32_e32 v64, v64, v52
	v_pk_mul_f32 v[52:53], v[60:61], v[126:127] op_sel_hi:[1,0]
	v_mad_i64_i32 v[68:69], s[30:31], v56, s59, v[134:135]
	v_mul_f32_e32 v65, v67, v48
	v_mul_f32_e32 v48, 0xbfb8aa3b, v53
	v_mov_b32_e32 v56, v49
	v_exp_f32_e32 v60, v48
	v_pk_mul_f32 v[48:49], v[56:57], v[126:127] op_sel_hi:[1,0]
	v_mul_f32_e32 v61, v66, v65
	v_mul_f32_e32 v56, 0xbfb8aa3b, v49
	v_exp_f32_e32 v56, v56
	v_add_f32_e32 v57, 1.0, v60
	v_rcp_f32_e32 v60, v57
	v_mov_b32_e32 v57, v62
	v_add_f32_e32 v56, 1.0, v56
	v_rcp_f32_e32 v65, v56
	v_mov_b32_e32 v56, v54
	v_pk_mul_f32 v[56:57], v[56:57], v[126:127] op_sel_hi:[1,0]
	v_mul_f32_e32 v53, v53, v60
	v_mul_f32_e32 v54, 0xbfb8aa3b, v57
	v_exp_f32_e32 v54, v54
	v_mul_f32_e32 v60, v52, v53
	v_mov_b32_e32 v53, v58
	v_mul_f32_e32 v49, v49, v65
	v_add_f32_e32 v52, 1.0, v54
	v_rcp_f32_e32 v54, v52
	v_mov_b32_e32 v52, v50
	v_pk_mul_f32 v[52:53], v[52:53], v[126:127] op_sel_hi:[1,0]
	v_mul_f32_e32 v65, v48, v49
	v_mul_f32_e32 v50, 0xbfb8aa3b, v53
	v_exp_f32_e32 v50, v50
	v_mul_f32_e32 v48, v57, v54
	v_mul_f32_e32 v54, v56, v48
	v_mov_b32_e32 v62, v55
	v_add_f32_e32 v48, 1.0, v50
	v_rcp_f32_e32 v56, v48
	v_pk_mul_f32 v[48:49], v[62:63], v[126:127] op_sel_hi:[1,0]
	v_mov_b32_e32 v58, v51
	v_mul_f32_e32 v50, 0xbfb8aa3b, v49
	v_exp_f32_e32 v55, v50
	v_pk_mul_f32 v[50:51], v[58:59], v[126:127] op_sel_hi:[1,0]
	v_mul_f32_e32 v53, v53, v56
	v_mul_f32_e32 v57, 0xbfb8aa3b, v51
	v_exp_f32_e32 v57, v57
	v_add_f32_e32 v55, 1.0, v55
	v_rcp_f32_e32 v55, v55
	v_add_f32_e32 v56, 1.0, v57
	v_rcp_f32_e32 v56, v56
	v_mul_f32_e32 v49, v49, v55
	v_mul_f32_e32 v49, v48, v49
	v_mul_f32_e32 v57, v52, v53
	v_mul_f32_e32 v48, v51, v56
	v_mul_f32_e32 v51, v50, v48
	v_lshl_add_u64 v[52:53], v[68:69], 0, v[112:113]
	v_cvt_pk_bf16_f32 v48, v64, v60
	v_cvt_pk_bf16_f32 v49, v54, v49
	v_cvt_pk_bf16_f32 v50, v61, v65
	v_cvt_pk_bf16_f32 v51, v57, v51
	global_store_dwordx4 v[52:53], v[48:51], off
	s_nop 1
	v_mov_b32_e32 v48, v36
	v_mov_b32_e32 v49, v44
	v_pk_mul_f32 v[48:49], v[48:49], v[124:125] op_sel_hi:[1,0]
	v_mov_b32_e32 v50, v32
	v_mul_f32_e32 v36, 0xbfb8aa3b, v49
	v_mov_b32_e32 v51, v40
	v_exp_f32_e32 v36, v36
	v_pk_mul_f32 v[50:51], v[50:51], v[124:125] op_sel_hi:[1,0]
	v_mov_b32_e32 v44, v37
	v_mul_f32_e32 v32, 0xbfb8aa3b, v51
	v_exp_f32_e32 v32, v32
	v_add_f32_e32 v36, 1.0, v36
	v_rcp_f32_e32 v36, v36
	v_add_u32_e32 v40, 0x90, v138
	v_add_f32_e32 v32, 1.0, v32
	v_rcp_f32_e32 v32, v32
	v_mul_f32_e32 v36, v49, v36
	v_mul_f32_e32 v48, v48, v36
	v_pk_mul_f32 v[36:37], v[44:45], v[124:125] op_sel_hi:[1,0]
	v_mad_i64_i32 v[52:53], s[30:31], v40, s59, v[134:135]
	v_mul_f32_e32 v49, v51, v32
	v_mul_f32_e32 v32, 0xbfb8aa3b, v37
	v_mov_b32_e32 v40, v33
	v_exp_f32_e32 v44, v32
	v_pk_mul_f32 v[32:33], v[40:41], v[124:125] op_sel_hi:[1,0]
	v_mul_f32_e32 v45, v50, v49
	v_mul_f32_e32 v40, 0xbfb8aa3b, v33
	v_exp_f32_e32 v40, v40
	v_add_f32_e32 v41, 1.0, v44
	v_rcp_f32_e32 v44, v41
	v_mov_b32_e32 v41, v46
	v_add_f32_e32 v40, 1.0, v40
	v_rcp_f32_e32 v49, v40
	v_mov_b32_e32 v40, v38
	v_pk_mul_f32 v[40:41], v[40:41], v[124:125] op_sel_hi:[1,0]
	v_mul_f32_e32 v37, v37, v44
	v_mul_f32_e32 v38, 0xbfb8aa3b, v41
	v_exp_f32_e32 v38, v38
	v_mul_f32_e32 v44, v36, v37
	v_mov_b32_e32 v37, v42
	v_mul_f32_e32 v33, v33, v49
	v_add_f32_e32 v36, 1.0, v38
	v_rcp_f32_e32 v38, v36
	v_mov_b32_e32 v36, v34
	v_pk_mul_f32 v[36:37], v[36:37], v[124:125] op_sel_hi:[1,0]
	v_mul_f32_e32 v49, v32, v33
	v_mul_f32_e32 v34, 0xbfb8aa3b, v37
	v_exp_f32_e32 v34, v34
	v_mul_f32_e32 v32, v41, v38
	v_mul_f32_e32 v38, v40, v32
	v_mov_b32_e32 v46, v39
	v_add_f32_e32 v32, 1.0, v34
	v_rcp_f32_e32 v40, v32
	v_pk_mul_f32 v[32:33], v[46:47], v[124:125] op_sel_hi:[1,0]
	v_mov_b32_e32 v42, v35
	v_mul_f32_e32 v34, 0xbfb8aa3b, v33
	v_exp_f32_e32 v39, v34
	v_pk_mul_f32 v[34:35], v[42:43], v[124:125] op_sel_hi:[1,0]
	v_mul_f32_e32 v37, v37, v40
	v_mul_f32_e32 v41, 0xbfb8aa3b, v35
	v_exp_f32_e32 v41, v41
	v_add_f32_e32 v39, 1.0, v39
	v_rcp_f32_e32 v39, v39
	v_add_f32_e32 v40, 1.0, v41
	v_rcp_f32_e32 v40, v40
	v_mul_f32_e32 v33, v33, v39
	v_mul_f32_e32 v33, v32, v33
	v_mul_f32_e32 v41, v36, v37
	v_mul_f32_e32 v32, v35, v40
	v_mul_f32_e32 v35, v34, v32
	v_lshl_add_u64 v[36:37], v[52:53], 0, v[112:113]
	v_cvt_pk_bf16_f32 v32, v48, v44
	v_cvt_pk_bf16_f32 v33, v38, v33
	v_cvt_pk_bf16_f32 v34, v45, v49
	v_cvt_pk_bf16_f32 v35, v41, v35
	global_store_dwordx4 v[36:37], v[32:35], off
	s_nop 1
	v_mov_b32_e32 v32, v20
	v_mov_b32_e32 v33, v28
	v_pk_mul_f32 v[32:33], v[32:33], v[122:123] op_sel_hi:[1,0]
	v_mov_b32_e32 v34, v16
	v_mul_f32_e32 v20, 0xbfb8aa3b, v33
	v_mov_b32_e32 v35, v24
	v_exp_f32_e32 v20, v20
	v_pk_mul_f32 v[34:35], v[34:35], v[122:123] op_sel_hi:[1,0]
	v_mov_b32_e32 v28, v21
	v_mul_f32_e32 v16, 0xbfb8aa3b, v35
	v_exp_f32_e32 v16, v16
	v_add_f32_e32 v20, 1.0, v20
	v_rcp_f32_e32 v20, v20
	v_add_u32_e32 v24, 0xa0, v138
	v_add_f32_e32 v16, 1.0, v16
	v_rcp_f32_e32 v16, v16
	v_mul_f32_e32 v20, v33, v20
	v_mul_f32_e32 v32, v32, v20
	v_pk_mul_f32 v[20:21], v[28:29], v[122:123] op_sel_hi:[1,0]
	v_mad_i64_i32 v[36:37], s[30:31], v24, s59, v[134:135]
	v_mul_f32_e32 v33, v35, v16
	v_mul_f32_e32 v16, 0xbfb8aa3b, v21
	v_mov_b32_e32 v24, v17
	v_exp_f32_e32 v28, v16
	v_pk_mul_f32 v[16:17], v[24:25], v[122:123] op_sel_hi:[1,0]
	v_mul_f32_e32 v29, v34, v33
	v_mul_f32_e32 v24, 0xbfb8aa3b, v17
	v_exp_f32_e32 v24, v24
	v_add_f32_e32 v25, 1.0, v28
	v_rcp_f32_e32 v28, v25
	v_mov_b32_e32 v25, v30
	v_add_f32_e32 v24, 1.0, v24
	v_rcp_f32_e32 v33, v24
	v_mov_b32_e32 v24, v22
	v_pk_mul_f32 v[24:25], v[24:25], v[122:123] op_sel_hi:[1,0]
	v_mul_f32_e32 v21, v21, v28
	v_mul_f32_e32 v22, 0xbfb8aa3b, v25
	v_exp_f32_e32 v22, v22
	v_mul_f32_e32 v28, v20, v21
	v_mov_b32_e32 v21, v26
	v_mul_f32_e32 v17, v17, v33
	v_add_f32_e32 v20, 1.0, v22
	v_rcp_f32_e32 v22, v20
	v_mov_b32_e32 v20, v18
	v_pk_mul_f32 v[20:21], v[20:21], v[122:123] op_sel_hi:[1,0]
	v_mul_f32_e32 v33, v16, v17
	v_mul_f32_e32 v18, 0xbfb8aa3b, v21
	v_exp_f32_e32 v18, v18
	v_mul_f32_e32 v16, v25, v22
	v_mul_f32_e32 v22, v24, v16
	v_mov_b32_e32 v30, v23
	v_add_f32_e32 v16, 1.0, v18
	v_rcp_f32_e32 v24, v16
	v_pk_mul_f32 v[16:17], v[30:31], v[122:123] op_sel_hi:[1,0]
	v_mov_b32_e32 v26, v19
	v_mul_f32_e32 v18, 0xbfb8aa3b, v17
	v_exp_f32_e32 v23, v18
	v_pk_mul_f32 v[18:19], v[26:27], v[122:123] op_sel_hi:[1,0]
	v_mul_f32_e32 v21, v21, v24
	v_mul_f32_e32 v25, 0xbfb8aa3b, v19
	v_exp_f32_e32 v25, v25
	v_add_f32_e32 v23, 1.0, v23
	v_rcp_f32_e32 v23, v23
	v_add_f32_e32 v24, 1.0, v25
	v_rcp_f32_e32 v24, v24
	v_mul_f32_e32 v17, v17, v23
	v_mul_f32_e32 v17, v16, v17
	v_mul_f32_e32 v25, v20, v21
	v_mul_f32_e32 v16, v19, v24
	v_mul_f32_e32 v19, v18, v16
	v_lshl_add_u64 v[20:21], v[36:37], 0, v[112:113]
	v_cvt_pk_bf16_f32 v16, v32, v28
	v_cvt_pk_bf16_f32 v17, v22, v17
	v_cvt_pk_bf16_f32 v18, v29, v33
	v_cvt_pk_bf16_f32 v19, v25, v19
	global_store_dwordx4 v[20:21], v[16:19], off
	s_nop 1
	v_mov_b32_e32 v16, v4
	v_mov_b32_e32 v17, v12
	v_pk_mul_f32 v[16:17], v[16:17], v[120:121] op_sel_hi:[1,0]
	v_mov_b32_e32 v18, v0
	v_mul_f32_e32 v4, 0xbfb8aa3b, v17
	v_mov_b32_e32 v19, v8
	v_exp_f32_e32 v4, v4
	v_pk_mul_f32 v[18:19], v[18:19], v[120:121] op_sel_hi:[1,0]
	v_mov_b32_e32 v12, v5
	v_mul_f32_e32 v0, 0xbfb8aa3b, v19
	v_exp_f32_e32 v0, v0
	v_add_f32_e32 v4, 1.0, v4
	v_rcp_f32_e32 v4, v4
	v_add_u32_e32 v8, 0xb0, v138
	v_add_f32_e32 v0, 1.0, v0
	v_rcp_f32_e32 v0, v0
	v_mul_f32_e32 v4, v17, v4
	v_mul_f32_e32 v16, v16, v4
	v_pk_mul_f32 v[4:5], v[12:13], v[120:121] op_sel_hi:[1,0]
	v_mad_i64_i32 v[20:21], s[30:31], v8, s59, v[134:135]
	v_mul_f32_e32 v17, v19, v0
	v_mul_f32_e32 v0, 0xbfb8aa3b, v5
	v_mov_b32_e32 v8, v1
	v_exp_f32_e32 v12, v0
	v_pk_mul_f32 v[0:1], v[8:9], v[120:121] op_sel_hi:[1,0]
	v_mul_f32_e32 v13, v18, v17
	v_mul_f32_e32 v8, 0xbfb8aa3b, v1
	v_exp_f32_e32 v8, v8
	v_add_f32_e32 v9, 1.0, v12
	v_rcp_f32_e32 v12, v9
	v_mov_b32_e32 v9, v14
	v_add_f32_e32 v8, 1.0, v8
	v_rcp_f32_e32 v17, v8
	v_mov_b32_e32 v8, v6
	v_pk_mul_f32 v[8:9], v[8:9], v[120:121] op_sel_hi:[1,0]
	v_mul_f32_e32 v5, v5, v12
	v_mul_f32_e32 v6, 0xbfb8aa3b, v9
	v_exp_f32_e32 v6, v6
	v_mul_f32_e32 v12, v4, v5
	v_mov_b32_e32 v5, v10
	v_mul_f32_e32 v1, v1, v17
	v_add_f32_e32 v4, 1.0, v6
	v_rcp_f32_e32 v6, v4
	v_mov_b32_e32 v4, v2
	v_pk_mul_f32 v[4:5], v[4:5], v[120:121] op_sel_hi:[1,0]
	v_mul_f32_e32 v17, v0, v1
	v_mul_f32_e32 v2, 0xbfb8aa3b, v5
	v_exp_f32_e32 v2, v2
	v_mul_f32_e32 v0, v9, v6
	v_mul_f32_e32 v6, v8, v0
	v_mov_b32_e32 v14, v7
	v_add_f32_e32 v0, 1.0, v2
	v_rcp_f32_e32 v8, v0
	v_pk_mul_f32 v[0:1], v[14:15], v[120:121] op_sel_hi:[1,0]
	v_mov_b32_e32 v10, v3
	v_mul_f32_e32 v2, 0xbfb8aa3b, v1
	v_exp_f32_e32 v7, v2
	v_pk_mul_f32 v[2:3], v[10:11], v[120:121] op_sel_hi:[1,0]
	v_mul_f32_e32 v5, v5, v8
	v_mul_f32_e32 v9, 0xbfb8aa3b, v3
	v_exp_f32_e32 v9, v9
	v_add_f32_e32 v7, 1.0, v7
	v_rcp_f32_e32 v7, v7
	v_add_f32_e32 v8, 1.0, v9
	v_rcp_f32_e32 v8, v8
	v_mul_f32_e32 v1, v1, v7
	v_mul_f32_e32 v1, v0, v1
	v_mul_f32_e32 v9, v4, v5
	v_mul_f32_e32 v0, v3, v8
	v_mul_f32_e32 v3, v2, v0
	v_lshl_add_u64 v[4:5], v[20:21], 0, v[112:113]
	v_cvt_pk_bf16_f32 v0, v16, v12
	v_cvt_pk_bf16_f32 v1, v6, v1
	v_cvt_pk_bf16_f32 v2, v13, v17
	v_cvt_pk_bf16_f32 v3, v9, v3
	global_store_dwordx4 v[4:5], v[0:3], off
	s_cbranch_vccnz .LBB0_777
	s_andn2_b64 vcc, exec, s[12:13]
	s_cbranch_vccnz .LBB0_776
	s_barrier
	s_branch .LBB0_776

.LBB0_2052:
	s_add_u32 s6, s2, 0x26000000
	s_addc_u32 s7, s3, 0
	s_add_u32 s48, s2, 0x8000000
	s_mul_i32 s47, s44, 3
	s_addc_u32 s49, s3, 0
	v_mbcnt_lo_u32_b32 v8, -1, 0
	v_mbcnt_hi_u32_b32 v8, -1, v8
	s_cmp_lt_i32 s46, s47
	v_add_u32_e32 v0, s42, v8
	s_cselect_b64 s[8:9], -1, 0
	s_cmp_ge_i32 s46, s47
	v_readfirstlane_b32 s20, v0
	s_cbranch_scc1 .LBB0_2054
	s_mul_hi_i32 s12, s46, 0x55555556
	s_lshr_b32 s13, s12, 31
	s_add_i32 s64, s12, s13
	s_lshl_b32 s12, s64, 2
	s_add_i32 s12, s12, 0
	s_add_i32 s12, s12, 0x20400
	v_mov_b32_e32 v1, s12
	ds_read_b32 v1, v1
	s_mul_i32 s12, s64, -3
	s_add_i32 s28, s12, s46
	s_mov_b64 s[30:31], s[6:7]
	s_waitcnt lgkmcnt(0)
	v_readfirstlane_b32 s12, v1
	s_ashr_i32 s13, s12, 16
	s_lshl_b32 s14, s13, 2
	s_add_i32 s14, s14, 0
	s_add_i32 s14, s14, 0x20a00
	v_mov_b32_e32 v1, s14
	ds_read_b32 v1, v1
	s_lshl_b32 s12, s12, 8
	s_and_b32 s12, s12, 0xffff00
	s_lshl_b32 s14, s13, 15
	s_add_i32 s65, s14, s12
	s_waitcnt lgkmcnt(0)
	v_readfirstlane_b32 s14, v1
	s_sub_i32 s12, s14, s12
	s_mul_hi_i32 s15, s13, 0x180000
	s_mul_i32 s13, s13, 0x180000
	s_min_i32 s14, s12, 0x100
	s_mov_b32 s80, s14
	s_add_u32 s16, s48, s13
	s_addc_u32 s15, s49, s15
	s_ashr_i32 s29, s28, 31
	s_lshl_b64 s[12:13], s[28:29], 19
	s_add_u32 s36, s16, s12
	s_addc_u32 s37, s15, s13
	s_andn2_b64 vcc, exec, s[8:9]
	s_cbranch_vccz .LBB0_2055
	s_branch .LBB0_2088

.LBB0_3036:
	s_add_u32 s6, s2, 0x26000000
	s_addc_u32 s7, s3, 0
	s_add_u32 s48, s2, 0xe000000
	s_mul_i32 s47, s44, 3
	s_addc_u32 s49, s3, 0
	v_mbcnt_lo_u32_b32 v8, -1, 0
	v_mbcnt_hi_u32_b32 v8, -1, v8
	s_cmp_lt_i32 s46, s47
	v_add_u32_e32 v0, s42, v8
	s_cselect_b64 s[8:9], -1, 0
	s_cmp_ge_i32 s46, s47
	v_readfirstlane_b32 s20, v0
	s_cbranch_scc1 .LBB0_3038
	s_mul_hi_i32 s12, s46, 0x55555556
	s_lshr_b32 s13, s12, 31
	s_add_i32 s64, s12, s13
	s_lshl_b32 s12, s64, 2
	s_add_i32 s12, s12, 0
	s_add_i32 s12, s12, 0x20400
	v_mov_b32_e32 v1, s12
	ds_read_b32 v1, v1
	s_mul_i32 s12, s64, -3
	s_add_i32 s28, s12, s46
	s_mov_b64 s[30:31], s[6:7]
	s_waitcnt lgkmcnt(0)
	v_readfirstlane_b32 s12, v1
	s_ashr_i32 s13, s12, 16
	s_lshl_b32 s14, s13, 2
	s_add_i32 s14, s14, 0
	s_add_i32 s14, s14, 0x20a00
	v_mov_b32_e32 v1, s14
	ds_read_b32 v1, v1
	s_lshl_b32 s12, s12, 8
	s_and_b32 s12, s12, 0xffff00
	s_lshl_b32 s14, s13, 15
	s_add_i32 s65, s14, s12
	s_waitcnt lgkmcnt(0)
	v_readfirstlane_b32 s14, v1
	s_sub_i32 s12, s14, s12
	s_mul_hi_i32 s15, s13, 0x180000
	s_mul_i32 s13, s13, 0x180000
	s_min_i32 s14, s12, 0x100
	s_mov_b32 s80, s14
	s_add_u32 s16, s48, s13
	s_addc_u32 s15, s49, s15
	s_ashr_i32 s29, s28, 31
	s_lshl_b64 s[12:13], s[28:29], 19
	s_add_u32 s36, s16, s12
	s_addc_u32 s37, s15, s13
	s_andn2_b64 vcc, exec, s[8:9]
	s_cbranch_vccz .LBB0_3039
	s_branch .LBB0_3072

.LBB0_4326:
	s_add_u32 s6, s2, 0x26000000
	s_addc_u32 s7, s3, 0
	s_add_u32 s47, s2, 0x14000000
	s_mul_i32 s46, s46, 3
	s_addc_u32 s48, s3, 0
	v_mbcnt_lo_u32_b32 v8, -1, 0
	v_mbcnt_hi_u32_b32 v8, -1, v8
	s_cmp_lt_i32 s45, s46
	v_add_u32_e32 v0, s42, v8
	s_cselect_b64 s[8:9], -1, 0
	s_cmp_ge_i32 s45, s46
	v_readfirstlane_b32 s20, v0
	s_cbranch_scc1 .LBB0_4328
	s_mul_hi_i32 s12, s45, 0x55555556
	s_lshr_b32 s13, s12, 31
	s_add_i32 s63, s12, s13
	s_lshl_b32 s12, s63, 2
	s_add_i32 s12, s12, 0
	s_add_i32 s12, s12, 0x20400
	v_mov_b32_e32 v1, s12
	ds_read_b32 v1, v1
	s_mul_i32 s12, s63, -3
	s_add_i32 s28, s12, s45
	s_mov_b64 s[30:31], s[6:7]
	s_waitcnt lgkmcnt(0)
	v_readfirstlane_b32 s12, v1
	s_ashr_i32 s13, s12, 16
	s_lshl_b32 s14, s13, 2
	s_add_i32 s14, s14, 0
	s_add_i32 s14, s14, 0x20a00
	v_mov_b32_e32 v1, s14
	ds_read_b32 v1, v1
	s_lshl_b32 s12, s12, 8
	s_and_b32 s12, s12, 0xffff00
	s_lshl_b32 s14, s13, 15
	s_add_i32 s64, s14, s12
	s_waitcnt lgkmcnt(0)
	v_readfirstlane_b32 s14, v1
	s_sub_i32 s12, s14, s12
	s_mul_hi_i32 s15, s13, 0x180000
	s_mul_i32 s13, s13, 0x180000
	s_min_i32 s14, s12, 0x100
	s_mov_b32 s80, s14
	s_add_u32 s16, s47, s13
	s_addc_u32 s15, s48, s15
	s_ashr_i32 s29, s28, 31
	s_lshl_b64 s[12:13], s[28:29], 19
	s_add_u32 s36, s16, s12
	s_addc_u32 s37, s15, s13
	s_andn2_b64 vcc, exec, s[8:9]
	s_cbranch_vccz .LBB0_4329
	s_branch .LBB0_4362

.LBB0_4341:
	s_andn2_b64 vcc, exec, s[2:3]
	s_mov_b32 s80, s62
	v_mov_b32_e32 v140, v158
	v_mov_b32_e32 v134, v155
	v_mov_b32_e32 v136, v156
	v_mov_b32_e32 v138, v157
	s_mov_b32 s64, s61
	s_mov_b32 s28, s22
	s_mov_b32 s63, s60
	s_mov_b64 s[36:37], s[24:25]
	s_mov_b64 s[30:31], s[26:27]
	s_cbranch_vccz .LBB0_4361

.LBB0_4358:
	s_add_i32 s81, s64, s80
	s_add_i32 s81, s81, -1
	v_add_u32_e32 v140, s64, v137
	v_min_i32_e32 v140, s81, v140
	v_ashrrev_i32_e32 v141, 31, v140
	v_lshl_add_u64 v[134:135], v[140:141], 2, s[16:17]
	global_load_dword v142, v[134:135], off
	v_mov_b32_e32 v162, v120
	v_add_u32_e32 v120, 16, v140
	v_mov_b32_e32 v163, v112
	v_mov_b32_e32 v112, v121
	v_min_i32_e32 v120, s81, v120
	v_ashrrev_i32_e32 v121, 31, v120
	v_lshl_add_u64 v[120:121], v[120:121], 2, s[16:17]
	global_load_dword v174, v[120:121], off
	v_mov_b32_e32 v160, v124
	v_mov_b32_e32 v164, v126
	v_mov_b32_e32 v166, v122
	v_add_u32_e32 v122, 32, v140
	v_add_u32_e32 v124, 48, v140
	v_add_u32_e32 v126, 0x80, v140
	v_mov_b32_e32 v161, v116
	v_mov_b32_e32 v116, v125
	v_mov_b32_e32 v165, v118
	v_mov_b32_e32 v167, v114
	v_mov_b32_e32 v118, v127
	v_mov_b32_e32 v114, v123
	v_add_u32_e32 v168, 0x90, v140
	v_add_u32_e32 v170, 0xa0, v140
	v_add_u32_e32 v140, 0xb0, v140
	v_min_i32_e32 v122, s81, v122
	v_ashrrev_i32_e32 v123, 31, v122
	v_min_i32_e32 v124, s81, v124
	v_ashrrev_i32_e32 v125, 31, v124
	v_min_i32_e32 v126, s81, v126
	v_ashrrev_i32_e32 v127, 31, v126
	v_min_i32_e32 v168, s81, v168
	v_ashrrev_i32_e32 v169, 31, v168
	v_min_i32_e32 v170, s81, v170
	v_ashrrev_i32_e32 v171, 31, v170
	v_min_i32_e32 v140, s81, v140
	v_ashrrev_i32_e32 v141, 31, v140
	v_lshl_add_u64 v[120:121], v[122:123], 2, s[16:17]
	v_lshl_add_u64 v[122:123], v[124:125], 2, s[16:17]
	v_lshl_add_u64 v[124:125], v[126:127], 2, s[16:17]
	v_lshl_add_u64 v[168:169], v[168:169], 2, s[16:17]
	v_lshl_add_u64 v[170:171], v[170:171], 2, s[16:17]
	v_lshl_add_u64 v[140:141], v[140:141], 2, s[16:17]
	global_load_dword v136, v[120:121], off
	global_load_dword v132, v[122:123], off
	global_load_dword v126, v[124:125], off
	s_nop 0
	global_load_dword v124, v[168:169], off
	global_load_dword v122, v[170:171], off
	global_load_dword v120, v[140:141], off
	v_lshl_or_b32 v144, s28, 7, v151
	v_lshl_add_u32 v138, s63, 8, v137
	v_mov_b64_e32 v[134:135], s[14:15]
	v_ashrrev_i32_e32 v145, 31, v144
	v_mad_i64_i32 v[172:173], s[30:31], v138, s58, v[134:135]
	s_and_b64 vcc, exec, s[2:3]
	s_mov_b64 s[2:3], -1
	s_waitcnt vmcnt(0)
	v_pk_mul_f32 v[116:117], v[116:117], v[142:143] op_sel_hi:[1,0]
	v_pk_mul_f32 v[112:113], v[112:113], v[142:143] op_sel_hi:[1,0]
	v_mul_f32_e32 v125, 0xbfb8aa3b, v117
	v_mul_f32_e32 v127, 0xbfb8aa3b, v113
	v_exp_f32_e32 v125, v125
	v_exp_f32_e32 v127, v127
	v_pk_mul_f32 v[140:141], v[160:161], v[142:143] op_sel_hi:[1,0]
	v_pk_mul_f32 v[160:161], v[162:163], v[142:143] op_sel_hi:[1,0]
	v_pk_mul_f32 v[162:163], v[164:165], v[142:143] op_sel_hi:[1,0]
	v_pk_mul_f32 v[164:165], v[166:167], v[142:143] op_sel_hi:[1,0]
	v_pk_mul_f32 v[118:119], v[118:119], v[142:143] op_sel_hi:[1,0]
	v_pk_mul_f32 v[114:115], v[114:115], v[142:143] op_sel_hi:[1,0]
	v_mul_f32_e32 v121, 0xbfb8aa3b, v141
	v_mul_f32_e32 v143, 0xbfb8aa3b, v165
	v_add_f32_e32 v125, 1.0, v125
	v_add_f32_e32 v127, 1.0, v127
	v_mul_f32_e32 v159, 0xbfb8aa3b, v119
	v_exp_f32_e32 v121, v121
	v_exp_f32_e32 v143, v143
	v_rcp_f32_e32 v125, v125
	v_rcp_f32_e32 v127, v127
	v_mul_f32_e32 v166, 0xbfb8aa3b, v115
	v_exp_f32_e32 v159, v159
	v_mul_f32_e32 v142, 0xbfb8aa3b, v163
	v_exp_f32_e32 v166, v166
	v_mul_f32_e32 v123, 0xbfb8aa3b, v161
	v_exp_f32_e32 v142, v142
	v_exp_f32_e32 v123, v123
	v_add_f32_e32 v121, 1.0, v121
	v_add_f32_e32 v143, 1.0, v143
	v_mul_f32_e32 v117, v117, v125
	v_mul_f32_e32 v113, v113, v127
	v_rcp_f32_e32 v121, v121
	v_rcp_f32_e32 v143, v143
	v_mul_f32_e32 v116, v116, v117
	v_mul_f32_e32 v117, v112, v113
	v_add_f32_e32 v113, 1.0, v159
	v_rcp_f32_e32 v113, v113
	v_add_f32_e32 v127, 1.0, v166
	v_add_f32_e32 v142, 1.0, v142
	v_rcp_f32_e32 v127, v127
	v_add_f32_e32 v123, 1.0, v123
	v_rcp_f32_e32 v142, v142
	v_rcp_f32_e32 v123, v123
	v_mul_f32_e32 v121, v141, v121
	v_mul_f32_e32 v112, v165, v143
	v_mul_f32_e32 v121, v140, v121
	v_mul_f32_e32 v140, v164, v112
	v_mul_f32_e32 v112, v119, v113
	v_mul_f32_e32 v141, v118, v112
	v_mul_f32_e32 v112, v115, v127
	v_mul_f32_e32 v125, v163, v142
	v_mul_f32_e32 v127, v114, v112
	v_lshlrev_b64 v[112:113], 1, v[144:145]
	v_mul_f32_e32 v123, v161, v123
	v_mul_f32_e32 v125, v162, v125
	v_lshl_add_u64 v[118:119], v[172:173], 0, v[112:113]
	v_cvt_pk_bf16_f32 v114, v121, v116
	v_cvt_pk_bf16_f32 v115, v125, v141
	v_mul_f32_e32 v123, v160, v123
	v_cvt_pk_bf16_f32 v116, v123, v117
	v_cvt_pk_bf16_f32 v117, v140, v127
	global_store_dwordx4 v[118:119], v[114:117], off
	s_nop 1
	v_mov_b32_e32 v114, v100
	v_mov_b32_e32 v115, v108
	v_pk_mul_f32 v[114:115], v[114:115], v[174:175] op_sel_hi:[1,0]
	v_mov_b32_e32 v116, v96
	v_mul_f32_e32 v100, 0xbfb8aa3b, v115
	v_mov_b32_e32 v117, v104
	v_exp_f32_e32 v100, v100
	v_pk_mul_f32 v[116:117], v[116:117], v[174:175] op_sel_hi:[1,0]
	v_mov_b32_e32 v108, v101
	v_mul_f32_e32 v96, 0xbfb8aa3b, v117
	v_exp_f32_e32 v96, v96
	v_add_f32_e32 v100, 1.0, v100
	v_rcp_f32_e32 v100, v100
	v_or_b32_e32 v104, 16, v138
	v_add_f32_e32 v96, 1.0, v96
	v_rcp_f32_e32 v96, v96
	v_mul_f32_e32 v100, v115, v100
	v_mul_f32_e32 v114, v114, v100
	v_pk_mul_f32 v[100:101], v[108:109], v[174:175] op_sel_hi:[1,0]
	v_mad_i64_i32 v[118:119], s[30:31], v104, s58, v[134:135]
	v_mul_f32_e32 v115, v117, v96
	v_mul_f32_e32 v96, 0xbfb8aa3b, v101
	v_mov_b32_e32 v104, v97
	v_exp_f32_e32 v108, v96
	v_pk_mul_f32 v[96:97], v[104:105], v[174:175] op_sel_hi:[1,0]
	v_mul_f32_e32 v109, v116, v115
	v_mul_f32_e32 v104, 0xbfb8aa3b, v97
	v_exp_f32_e32 v104, v104
	v_add_f32_e32 v105, 1.0, v108
	v_rcp_f32_e32 v108, v105
	v_mov_b32_e32 v105, v110
	v_add_f32_e32 v104, 1.0, v104
	v_rcp_f32_e32 v115, v104
	v_mov_b32_e32 v104, v102
	v_pk_mul_f32 v[104:105], v[104:105], v[174:175] op_sel_hi:[1,0]
	v_mul_f32_e32 v101, v101, v108
	v_mul_f32_e32 v102, 0xbfb8aa3b, v105
	v_exp_f32_e32 v102, v102
	v_mul_f32_e32 v108, v100, v101
	v_mov_b32_e32 v101, v106
	v_mul_f32_e32 v97, v97, v115
	v_add_f32_e32 v100, 1.0, v102
	v_rcp_f32_e32 v102, v100
	v_mov_b32_e32 v100, v98
	v_pk_mul_f32 v[100:101], v[100:101], v[174:175] op_sel_hi:[1,0]
	v_mul_f32_e32 v115, v96, v97
	v_mul_f32_e32 v98, 0xbfb8aa3b, v101
	v_exp_f32_e32 v98, v98
	v_mul_f32_e32 v96, v105, v102
	v_mul_f32_e32 v102, v104, v96
	v_mov_b32_e32 v110, v103
	v_add_f32_e32 v96, 1.0, v98
	v_rcp_f32_e32 v104, v96
	v_pk_mul_f32 v[96:97], v[110:111], v[174:175] op_sel_hi:[1,0]
	v_mov_b32_e32 v106, v99
	v_mul_f32_e32 v98, 0xbfb8aa3b, v97
	v_exp_f32_e32 v103, v98
	v_pk_mul_f32 v[98:99], v[106:107], v[174:175] op_sel_hi:[1,0]
	v_mul_f32_e32 v101, v101, v104
	v_mul_f32_e32 v105, 0xbfb8aa3b, v99
	v_exp_f32_e32 v105, v105
	v_add_f32_e32 v103, 1.0, v103
	v_rcp_f32_e32 v103, v103
	v_add_f32_e32 v104, 1.0, v105
	v_rcp_f32_e32 v104, v104
	v_mul_f32_e32 v97, v97, v103
	v_mul_f32_e32 v97, v96, v97
	v_mul_f32_e32 v105, v100, v101
	v_mul_f32_e32 v96, v99, v104
	v_mul_f32_e32 v99, v98, v96
	v_lshl_add_u64 v[100:101], v[118:119], 0, v[112:113]
	v_cvt_pk_bf16_f32 v96, v114, v108
	v_cvt_pk_bf16_f32 v97, v102, v97
	v_cvt_pk_bf16_f32 v98, v109, v115
	v_cvt_pk_bf16_f32 v99, v105, v99
	global_store_dwordx4 v[100:101], v[96:99], off
	s_nop 1
	v_mov_b32_e32 v96, v84
	v_mov_b32_e32 v97, v92
	v_pk_mul_f32 v[96:97], v[96:97], v[136:137] op_sel_hi:[1,0]
	v_mov_b32_e32 v98, v80
	v_mul_f32_e32 v84, 0xbfb8aa3b, v97
	v_mov_b32_e32 v99, v88
	v_exp_f32_e32 v84, v84
	v_pk_mul_f32 v[98:99], v[98:99], v[136:137] op_sel_hi:[1,0]
	v_mov_b32_e32 v92, v85
	v_mul_f32_e32 v80, 0xbfb8aa3b, v99
	v_exp_f32_e32 v80, v80
	v_add_f32_e32 v84, 1.0, v84
	v_rcp_f32_e32 v84, v84
	v_or_b32_e32 v88, 32, v138
	v_add_f32_e32 v80, 1.0, v80
	v_rcp_f32_e32 v80, v80
	v_mul_f32_e32 v84, v97, v84
	v_mul_f32_e32 v96, v96, v84
	v_pk_mul_f32 v[84:85], v[92:93], v[136:137] op_sel_hi:[1,0]
	v_mad_i64_i32 v[100:101], s[30:31], v88, s58, v[134:135]
	v_mul_f32_e32 v97, v99, v80
	v_mul_f32_e32 v80, 0xbfb8aa3b, v85
	v_mov_b32_e32 v88, v81
	v_exp_f32_e32 v92, v80
	v_pk_mul_f32 v[80:81], v[88:89], v[136:137] op_sel_hi:[1,0]
	v_mul_f32_e32 v93, v98, v97
	v_mul_f32_e32 v88, 0xbfb8aa3b, v81
	v_exp_f32_e32 v88, v88
	v_add_f32_e32 v89, 1.0, v92
	v_rcp_f32_e32 v92, v89
	v_mov_b32_e32 v89, v94
	v_add_f32_e32 v88, 1.0, v88
	v_rcp_f32_e32 v97, v88
	v_mov_b32_e32 v88, v86
	v_pk_mul_f32 v[88:89], v[88:89], v[136:137] op_sel_hi:[1,0]
	v_mul_f32_e32 v85, v85, v92
	v_mul_f32_e32 v86, 0xbfb8aa3b, v89
	v_exp_f32_e32 v86, v86
	v_mul_f32_e32 v92, v84, v85
	v_mov_b32_e32 v85, v90
	v_mul_f32_e32 v81, v81, v97
	v_add_f32_e32 v84, 1.0, v86
	v_rcp_f32_e32 v86, v84
	v_mov_b32_e32 v84, v82
	v_pk_mul_f32 v[84:85], v[84:85], v[136:137] op_sel_hi:[1,0]
	v_mul_f32_e32 v97, v80, v81
	v_mul_f32_e32 v82, 0xbfb8aa3b, v85
	v_exp_f32_e32 v82, v82
	v_mul_f32_e32 v80, v89, v86
	v_mul_f32_e32 v86, v88, v80
	v_mov_b32_e32 v94, v87
	v_add_f32_e32 v80, 1.0, v82
	v_rcp_f32_e32 v88, v80
	v_pk_mul_f32 v[80:81], v[94:95], v[136:137] op_sel_hi:[1,0]
	v_mov_b32_e32 v90, v83
	v_mul_f32_e32 v82, 0xbfb8aa3b, v81
	v_exp_f32_e32 v87, v82
	v_pk_mul_f32 v[82:83], v[90:91], v[136:137] op_sel_hi:[1,0]
	v_mul_f32_e32 v85, v85, v88
	v_mul_f32_e32 v89, 0xbfb8aa3b, v83
	v_exp_f32_e32 v89, v89
	v_add_f32_e32 v87, 1.0, v87
	v_rcp_f32_e32 v87, v87
	v_add_f32_e32 v88, 1.0, v89
	v_rcp_f32_e32 v88, v88
	v_mul_f32_e32 v81, v81, v87
	v_mul_f32_e32 v81, v80, v81
	v_mul_f32_e32 v89, v84, v85
	v_mul_f32_e32 v80, v83, v88
	v_mul_f32_e32 v83, v82, v80
	v_lshl_add_u64 v[84:85], v[100:101], 0, v[112:113]
	v_cvt_pk_bf16_f32 v80, v96, v92
	v_cvt_pk_bf16_f32 v81, v86, v81
	v_cvt_pk_bf16_f32 v82, v93, v97
	v_cvt_pk_bf16_f32 v83, v89, v83
	global_store_dwordx4 v[84:85], v[80:83], off
	s_nop 1
	v_mov_b32_e32 v80, v68
	v_mov_b32_e32 v81, v76
	v_pk_mul_f32 v[80:81], v[80:81], v[132:133] op_sel_hi:[1,0]
	v_mov_b32_e32 v82, v64
	v_mul_f32_e32 v68, 0xbfb8aa3b, v81
	v_mov_b32_e32 v83, v72
	v_exp_f32_e32 v68, v68
	v_pk_mul_f32 v[82:83], v[82:83], v[132:133] op_sel_hi:[1,0]
	v_mov_b32_e32 v76, v69
	v_mul_f32_e32 v64, 0xbfb8aa3b, v83
	v_exp_f32_e32 v64, v64
	v_add_f32_e32 v68, 1.0, v68
	v_rcp_f32_e32 v68, v68
	v_or_b32_e32 v72, 48, v138
	v_add_f32_e32 v64, 1.0, v64
	v_rcp_f32_e32 v64, v64
	v_mul_f32_e32 v68, v81, v68
	v_mul_f32_e32 v80, v80, v68
	v_pk_mul_f32 v[68:69], v[76:77], v[132:133] op_sel_hi:[1,0]
	v_mad_i64_i32 v[84:85], s[30:31], v72, s58, v[134:135]
	v_mul_f32_e32 v81, v83, v64
	v_mul_f32_e32 v64, 0xbfb8aa3b, v69
	v_mov_b32_e32 v72, v65
	v_exp_f32_e32 v76, v64
	v_pk_mul_f32 v[64:65], v[72:73], v[132:133] op_sel_hi:[1,0]
	v_mul_f32_e32 v77, v82, v81
	v_mul_f32_e32 v72, 0xbfb8aa3b, v65
	v_exp_f32_e32 v72, v72
	v_add_f32_e32 v73, 1.0, v76
	v_rcp_f32_e32 v76, v73
	v_mov_b32_e32 v73, v78
	v_add_f32_e32 v72, 1.0, v72
	v_rcp_f32_e32 v81, v72
	v_mov_b32_e32 v72, v70
	v_pk_mul_f32 v[72:73], v[72:73], v[132:133] op_sel_hi:[1,0]
	v_mul_f32_e32 v69, v69, v76
	v_mul_f32_e32 v70, 0xbfb8aa3b, v73
	v_exp_f32_e32 v70, v70
	v_mul_f32_e32 v76, v68, v69
	v_mov_b32_e32 v69, v74
	v_mul_f32_e32 v65, v65, v81
	v_add_f32_e32 v68, 1.0, v70
	v_rcp_f32_e32 v70, v68
	v_mov_b32_e32 v68, v66
	v_pk_mul_f32 v[68:69], v[68:69], v[132:133] op_sel_hi:[1,0]
	v_mul_f32_e32 v81, v64, v65
	v_mul_f32_e32 v66, 0xbfb8aa3b, v69
	v_exp_f32_e32 v66, v66
	v_mul_f32_e32 v64, v73, v70
	v_mul_f32_e32 v70, v72, v64
	v_mov_b32_e32 v78, v71
	v_add_f32_e32 v64, 1.0, v66
	v_rcp_f32_e32 v72, v64
	v_pk_mul_f32 v[64:65], v[78:79], v[132:133] op_sel_hi:[1,0]
	v_mov_b32_e32 v74, v67
	v_mul_f32_e32 v66, 0xbfb8aa3b, v65
	v_exp_f32_e32 v71, v66
	v_pk_mul_f32 v[66:67], v[74:75], v[132:133] op_sel_hi:[1,0]
	v_mul_f32_e32 v69, v69, v72
	v_mul_f32_e32 v73, 0xbfb8aa3b, v67
	v_exp_f32_e32 v73, v73
	v_add_f32_e32 v71, 1.0, v71
	v_rcp_f32_e32 v71, v71
	v_add_f32_e32 v72, 1.0, v73
	v_rcp_f32_e32 v72, v72
	v_mul_f32_e32 v65, v65, v71
	v_mul_f32_e32 v65, v64, v65
	v_mul_f32_e32 v73, v68, v69
	v_mul_f32_e32 v64, v67, v72
	v_mul_f32_e32 v67, v66, v64
	v_lshl_add_u64 v[68:69], v[84:85], 0, v[112:113]
	v_cvt_pk_bf16_f32 v64, v80, v76
	v_cvt_pk_bf16_f32 v65, v70, v65
	v_cvt_pk_bf16_f32 v66, v77, v81
	v_cvt_pk_bf16_f32 v67, v73, v67
	global_store_dwordx4 v[68:69], v[64:67], off
	s_nop 1
	v_mov_b32_e32 v64, v52
	v_mov_b32_e32 v65, v60
	v_pk_mul_f32 v[64:65], v[64:65], v[126:127] op_sel_hi:[1,0]
	v_mov_b32_e32 v66, v48
	v_mul_f32_e32 v52, 0xbfb8aa3b, v65
	v_mov_b32_e32 v67, v56
	v_exp_f32_e32 v52, v52
	v_pk_mul_f32 v[66:67], v[66:67], v[126:127] op_sel_hi:[1,0]
	v_mov_b32_e32 v60, v53
	v_mul_f32_e32 v48, 0xbfb8aa3b, v67
	v_exp_f32_e32 v48, v48
	v_add_f32_e32 v52, 1.0, v52
	v_rcp_f32_e32 v52, v52
	v_add_u32_e32 v56, 0x80, v138
	v_add_f32_e32 v48, 1.0, v48
	v_rcp_f32_e32 v48, v48
	v_mul_f32_e32 v52, v65, v52
	v_mul_f32_e32 v64, v64, v52
	v_pk_mul_f32 v[52:53], v[60:61], v[126:127] op_sel_hi:[1,0]
	v_mad_i64_i32 v[68:69], s[30:31], v56, s58, v[134:135]
	v_mul_f32_e32 v65, v67, v48
	v_mul_f32_e32 v48, 0xbfb8aa3b, v53
	v_mov_b32_e32 v56, v49
	v_exp_f32_e32 v60, v48
	v_pk_mul_f32 v[48:49], v[56:57], v[126:127] op_sel_hi:[1,0]
	v_mul_f32_e32 v61, v66, v65
	v_mul_f32_e32 v56, 0xbfb8aa3b, v49
	v_exp_f32_e32 v56, v56
	v_add_f32_e32 v57, 1.0, v60
	v_rcp_f32_e32 v60, v57
	v_mov_b32_e32 v57, v62
	v_add_f32_e32 v56, 1.0, v56
	v_rcp_f32_e32 v65, v56
	v_mov_b32_e32 v56, v54
	v_pk_mul_f32 v[56:57], v[56:57], v[126:127] op_sel_hi:[1,0]
	v_mul_f32_e32 v53, v53, v60
	v_mul_f32_e32 v54, 0xbfb8aa3b, v57
	v_exp_f32_e32 v54, v54
	v_mul_f32_e32 v60, v52, v53
	v_mov_b32_e32 v53, v58
	v_mul_f32_e32 v49, v49, v65
	v_add_f32_e32 v52, 1.0, v54
	v_rcp_f32_e32 v54, v52
	v_mov_b32_e32 v52, v50
	v_pk_mul_f32 v[52:53], v[52:53], v[126:127] op_sel_hi:[1,0]
	v_mul_f32_e32 v65, v48, v49
	v_mul_f32_e32 v50, 0xbfb8aa3b, v53
	v_exp_f32_e32 v50, v50
	v_mul_f32_e32 v48, v57, v54
	v_mul_f32_e32 v54, v56, v48
	v_mov_b32_e32 v62, v55
	v_add_f32_e32 v48, 1.0, v50
	v_rcp_f32_e32 v56, v48
	v_pk_mul_f32 v[48:49], v[62:63], v[126:127] op_sel_hi:[1,0]
	v_mov_b32_e32 v58, v51
	v_mul_f32_e32 v50, 0xbfb8aa3b, v49
	v_exp_f32_e32 v55, v50
	v_pk_mul_f32 v[50:51], v[58:59], v[126:127] op_sel_hi:[1,0]
	v_mul_f32_e32 v53, v53, v56
	v_mul_f32_e32 v57, 0xbfb8aa3b, v51
	v_exp_f32_e32 v57, v57
	v_add_f32_e32 v55, 1.0, v55
	v_rcp_f32_e32 v55, v55
	v_add_f32_e32 v56, 1.0, v57
	v_rcp_f32_e32 v56, v56
	v_mul_f32_e32 v49, v49, v55
	v_mul_f32_e32 v49, v48, v49
	v_mul_f32_e32 v57, v52, v53
	v_mul_f32_e32 v48, v51, v56
	v_mul_f32_e32 v51, v50, v48
	v_lshl_add_u64 v[52:53], v[68:69], 0, v[112:113]
	v_cvt_pk_bf16_f32 v48, v64, v60
	v_cvt_pk_bf16_f32 v49, v54, v49
	v_cvt_pk_bf16_f32 v50, v61, v65
	v_cvt_pk_bf16_f32 v51, v57, v51
	global_store_dwordx4 v[52:53], v[48:51], off
	s_nop 1
	v_mov_b32_e32 v48, v36
	v_mov_b32_e32 v49, v44
	v_pk_mul_f32 v[48:49], v[48:49], v[124:125] op_sel_hi:[1,0]
	v_mov_b32_e32 v50, v32
	v_mul_f32_e32 v36, 0xbfb8aa3b, v49
	v_mov_b32_e32 v51, v40
	v_exp_f32_e32 v36, v36
	v_pk_mul_f32 v[50:51], v[50:51], v[124:125] op_sel_hi:[1,0]
	v_mov_b32_e32 v44, v37
	v_mul_f32_e32 v32, 0xbfb8aa3b, v51
	v_exp_f32_e32 v32, v32
	v_add_f32_e32 v36, 1.0, v36
	v_rcp_f32_e32 v36, v36
	v_add_u32_e32 v40, 0x90, v138
	v_add_f32_e32 v32, 1.0, v32
	v_rcp_f32_e32 v32, v32
	v_mul_f32_e32 v36, v49, v36
	v_mul_f32_e32 v48, v48, v36
	v_pk_mul_f32 v[36:37], v[44:45], v[124:125] op_sel_hi:[1,0]
	v_mad_i64_i32 v[52:53], s[30:31], v40, s58, v[134:135]
	v_mul_f32_e32 v49, v51, v32
	v_mul_f32_e32 v32, 0xbfb8aa3b, v37
	v_mov_b32_e32 v40, v33
	v_exp_f32_e32 v44, v32
	v_pk_mul_f32 v[32:33], v[40:41], v[124:125] op_sel_hi:[1,0]
	v_mul_f32_e32 v45, v50, v49
	v_mul_f32_e32 v40, 0xbfb8aa3b, v33
	v_exp_f32_e32 v40, v40
	v_add_f32_e32 v41, 1.0, v44
	v_rcp_f32_e32 v44, v41
	v_mov_b32_e32 v41, v46
	v_add_f32_e32 v40, 1.0, v40
	v_rcp_f32_e32 v49, v40
	v_mov_b32_e32 v40, v38
	v_pk_mul_f32 v[40:41], v[40:41], v[124:125] op_sel_hi:[1,0]
	v_mul_f32_e32 v37, v37, v44
	v_mul_f32_e32 v38, 0xbfb8aa3b, v41
	v_exp_f32_e32 v38, v38
	v_mul_f32_e32 v44, v36, v37
	v_mov_b32_e32 v37, v42
	v_mul_f32_e32 v33, v33, v49
	v_add_f32_e32 v36, 1.0, v38
	v_rcp_f32_e32 v38, v36
	v_mov_b32_e32 v36, v34
	v_pk_mul_f32 v[36:37], v[36:37], v[124:125] op_sel_hi:[1,0]
	v_mul_f32_e32 v49, v32, v33
	v_mul_f32_e32 v34, 0xbfb8aa3b, v37
	v_exp_f32_e32 v34, v34
	v_mul_f32_e32 v32, v41, v38
	v_mul_f32_e32 v38, v40, v32
	v_mov_b32_e32 v46, v39
	v_add_f32_e32 v32, 1.0, v34
	v_rcp_f32_e32 v40, v32
	v_pk_mul_f32 v[32:33], v[46:47], v[124:125] op_sel_hi:[1,0]
	v_mov_b32_e32 v42, v35
	v_mul_f32_e32 v34, 0xbfb8aa3b, v33
	v_exp_f32_e32 v39, v34
	v_pk_mul_f32 v[34:35], v[42:43], v[124:125] op_sel_hi:[1,0]
	v_mul_f32_e32 v37, v37, v40
	v_mul_f32_e32 v41, 0xbfb8aa3b, v35
	v_exp_f32_e32 v41, v41
	v_add_f32_e32 v39, 1.0, v39
	v_rcp_f32_e32 v39, v39
	v_add_f32_e32 v40, 1.0, v41
	v_rcp_f32_e32 v40, v40
	v_mul_f32_e32 v33, v33, v39
	v_mul_f32_e32 v33, v32, v33
	v_mul_f32_e32 v41, v36, v37
	v_mul_f32_e32 v32, v35, v40
	v_mul_f32_e32 v35, v34, v32
	v_lshl_add_u64 v[36:37], v[52:53], 0, v[112:113]
	v_cvt_pk_bf16_f32 v32, v48, v44
	v_cvt_pk_bf16_f32 v33, v38, v33
	v_cvt_pk_bf16_f32 v34, v45, v49
	v_cvt_pk_bf16_f32 v35, v41, v35
	global_store_dwordx4 v[36:37], v[32:35], off
	s_nop 1
	v_mov_b32_e32 v32, v20
	v_mov_b32_e32 v33, v28
	v_pk_mul_f32 v[32:33], v[32:33], v[122:123] op_sel_hi:[1,0]
	v_mov_b32_e32 v34, v16
	v_mul_f32_e32 v20, 0xbfb8aa3b, v33
	v_mov_b32_e32 v35, v24
	v_exp_f32_e32 v20, v20
	v_pk_mul_f32 v[34:35], v[34:35], v[122:123] op_sel_hi:[1,0]
	v_mov_b32_e32 v28, v21
	v_mul_f32_e32 v16, 0xbfb8aa3b, v35
	v_exp_f32_e32 v16, v16
	v_add_f32_e32 v20, 1.0, v20
	v_rcp_f32_e32 v20, v20
	v_add_u32_e32 v24, 0xa0, v138
	v_add_f32_e32 v16, 1.0, v16
	v_rcp_f32_e32 v16, v16
	v_mul_f32_e32 v20, v33, v20
	v_mul_f32_e32 v32, v32, v20
	v_pk_mul_f32 v[20:21], v[28:29], v[122:123] op_sel_hi:[1,0]
	v_mad_i64_i32 v[36:37], s[30:31], v24, s58, v[134:135]
	v_mul_f32_e32 v33, v35, v16
	v_mul_f32_e32 v16, 0xbfb8aa3b, v21
	v_mov_b32_e32 v24, v17
	v_exp_f32_e32 v28, v16
	v_pk_mul_f32 v[16:17], v[24:25], v[122:123] op_sel_hi:[1,0]
	v_mul_f32_e32 v29, v34, v33
	v_mul_f32_e32 v24, 0xbfb8aa3b, v17
	v_exp_f32_e32 v24, v24
	v_add_f32_e32 v25, 1.0, v28
	v_rcp_f32_e32 v28, v25
	v_mov_b32_e32 v25, v30
	v_add_f32_e32 v24, 1.0, v24
	v_rcp_f32_e32 v33, v24
	v_mov_b32_e32 v24, v22
	v_pk_mul_f32 v[24:25], v[24:25], v[122:123] op_sel_hi:[1,0]
	v_mul_f32_e32 v21, v21, v28
	v_mul_f32_e32 v22, 0xbfb8aa3b, v25
	v_exp_f32_e32 v22, v22
	v_mul_f32_e32 v28, v20, v21
	v_mov_b32_e32 v21, v26
	v_mul_f32_e32 v17, v17, v33
	v_add_f32_e32 v20, 1.0, v22
	v_rcp_f32_e32 v22, v20
	v_mov_b32_e32 v20, v18
	v_pk_mul_f32 v[20:21], v[20:21], v[122:123] op_sel_hi:[1,0]
	v_mul_f32_e32 v33, v16, v17
	v_mul_f32_e32 v18, 0xbfb8aa3b, v21
	v_exp_f32_e32 v18, v18
	v_mul_f32_e32 v16, v25, v22
	v_mul_f32_e32 v22, v24, v16
	v_mov_b32_e32 v30, v23
	v_add_f32_e32 v16, 1.0, v18
	v_rcp_f32_e32 v24, v16
	v_pk_mul_f32 v[16:17], v[30:31], v[122:123] op_sel_hi:[1,0]
	v_mov_b32_e32 v26, v19
	v_mul_f32_e32 v18, 0xbfb8aa3b, v17
	v_exp_f32_e32 v23, v18
	v_pk_mul_f32 v[18:19], v[26:27], v[122:123] op_sel_hi:[1,0]
	v_mul_f32_e32 v21, v21, v24
	v_mul_f32_e32 v25, 0xbfb8aa3b, v19
	v_exp_f32_e32 v25, v25
	v_add_f32_e32 v23, 1.0, v23
	v_rcp_f32_e32 v23, v23
	v_add_f32_e32 v24, 1.0, v25
	v_rcp_f32_e32 v24, v24
	v_mul_f32_e32 v17, v17, v23
	v_mul_f32_e32 v17, v16, v17
	v_mul_f32_e32 v25, v20, v21
	v_mul_f32_e32 v16, v19, v24
	v_mul_f32_e32 v19, v18, v16
	v_lshl_add_u64 v[20:21], v[36:37], 0, v[112:113]
	v_cvt_pk_bf16_f32 v16, v32, v28
	v_cvt_pk_bf16_f32 v17, v22, v17
	v_cvt_pk_bf16_f32 v18, v29, v33
	v_cvt_pk_bf16_f32 v19, v25, v19
	global_store_dwordx4 v[20:21], v[16:19], off
	s_nop 1
	v_mov_b32_e32 v16, v4
	v_mov_b32_e32 v17, v12
	v_pk_mul_f32 v[16:17], v[16:17], v[120:121] op_sel_hi:[1,0]
	v_mov_b32_e32 v18, v0
	v_mul_f32_e32 v4, 0xbfb8aa3b, v17
	v_mov_b32_e32 v19, v8
	v_exp_f32_e32 v4, v4
	v_pk_mul_f32 v[18:19], v[18:19], v[120:121] op_sel_hi:[1,0]
	v_mov_b32_e32 v12, v5
	v_mul_f32_e32 v0, 0xbfb8aa3b, v19
	v_exp_f32_e32 v0, v0
	v_add_f32_e32 v4, 1.0, v4
	v_rcp_f32_e32 v4, v4
	v_add_u32_e32 v8, 0xb0, v138
	v_add_f32_e32 v0, 1.0, v0
	v_rcp_f32_e32 v0, v0
	v_mul_f32_e32 v4, v17, v4
	v_mul_f32_e32 v16, v16, v4
	v_pk_mul_f32 v[4:5], v[12:13], v[120:121] op_sel_hi:[1,0]
	v_mad_i64_i32 v[20:21], s[30:31], v8, s58, v[134:135]
	v_mul_f32_e32 v17, v19, v0
	v_mul_f32_e32 v0, 0xbfb8aa3b, v5
	v_mov_b32_e32 v8, v1
	v_exp_f32_e32 v12, v0
	v_pk_mul_f32 v[0:1], v[8:9], v[120:121] op_sel_hi:[1,0]
	v_mul_f32_e32 v13, v18, v17
	v_mul_f32_e32 v8, 0xbfb8aa3b, v1
	v_exp_f32_e32 v8, v8
	v_add_f32_e32 v9, 1.0, v12
	v_rcp_f32_e32 v12, v9
	v_mov_b32_e32 v9, v14
	v_add_f32_e32 v8, 1.0, v8
	v_rcp_f32_e32 v17, v8
	v_mov_b32_e32 v8, v6
	v_pk_mul_f32 v[8:9], v[8:9], v[120:121] op_sel_hi:[1,0]
	v_mul_f32_e32 v5, v5, v12
	v_mul_f32_e32 v6, 0xbfb8aa3b, v9
	v_exp_f32_e32 v6, v6
	v_mul_f32_e32 v12, v4, v5
	v_mov_b32_e32 v5, v10
	v_mul_f32_e32 v1, v1, v17
	v_add_f32_e32 v4, 1.0, v6
	v_rcp_f32_e32 v6, v4
	v_mov_b32_e32 v4, v2
	v_pk_mul_f32 v[4:5], v[4:5], v[120:121] op_sel_hi:[1,0]
	v_mul_f32_e32 v17, v0, v1
	v_mul_f32_e32 v2, 0xbfb8aa3b, v5
	v_exp_f32_e32 v2, v2
	v_mul_f32_e32 v0, v9, v6
	v_mul_f32_e32 v6, v8, v0
	v_mov_b32_e32 v14, v7
	v_add_f32_e32 v0, 1.0, v2
	v_rcp_f32_e32 v8, v0
	v_pk_mul_f32 v[0:1], v[14:15], v[120:121] op_sel_hi:[1,0]
	v_mov_b32_e32 v10, v3
	v_mul_f32_e32 v2, 0xbfb8aa3b, v1
	v_exp_f32_e32 v7, v2
	v_pk_mul_f32 v[2:3], v[10:11], v[120:121] op_sel_hi:[1,0]
	v_mul_f32_e32 v5, v5, v8
	v_mul_f32_e32 v9, 0xbfb8aa3b, v3
	v_exp_f32_e32 v9, v9
	v_add_f32_e32 v7, 1.0, v7
	v_rcp_f32_e32 v7, v7
	v_add_f32_e32 v8, 1.0, v9
	v_rcp_f32_e32 v8, v8
	v_mul_f32_e32 v1, v1, v7
	v_mul_f32_e32 v1, v0, v1
	v_mul_f32_e32 v9, v4, v5
	v_mul_f32_e32 v0, v3, v8
	v_mul_f32_e32 v3, v2, v0
	v_lshl_add_u64 v[4:5], v[20:21], 0, v[112:113]
	v_cvt_pk_bf16_f32 v0, v16, v12
	v_cvt_pk_bf16_f32 v1, v6, v1
	v_cvt_pk_bf16_f32 v2, v13, v17
	v_cvt_pk_bf16_f32 v3, v9, v3
	global_store_dwordx4 v[4:5], v[0:3], off
	s_cbranch_vccnz .LBB0_4341
	s_andn2_b64 vcc, exec, s[12:13]
	s_cbranch_vccnz .LBB0_4340
	s_barrier
	s_branch .LBB0_4340

	.amdhsa_kernel _Z3fwd4Args
		.amdhsa_group_segment_fixed_size 0
		.amdhsa_private_segment_fixed_size 0
		.amdhsa_kernarg_size 464
		.amdhsa_user_sgpr_count 2
		.amdhsa_user_sgpr_dispatch_ptr 0
		.amdhsa_user_sgpr_queue_ptr 0
		.amdhsa_user_sgpr_kernarg_segment_ptr 1
		.amdhsa_user_sgpr_dispatch_id 0
		.amdhsa_user_sgpr_kernarg_preload_length 0
		.amdhsa_user_sgpr_kernarg_preload_offset 0
		.amdhsa_user_sgpr_private_segment_size 0
		.amdhsa_uses_dynamic_stack 0
		.amdhsa_enable_private_segment 0
		.amdhsa_system_sgpr_workgroup_id_x 1
		.amdhsa_system_sgpr_workgroup_id_y 0
		.amdhsa_system_sgpr_workgroup_id_z 0
		.amdhsa_system_sgpr_workgroup_info 0
		.amdhsa_system_vgpr_workitem_id 0
		.amdhsa_next_free_vgpr 256
		.amdhsa_next_free_sgpr 88
		.amdhsa_accum_offset 256
		.amdhsa_reserve_vcc 1
		.amdhsa_float_round_mode_32 0
		.amdhsa_float_round_mode_16_64 0
		.amdhsa_float_denorm_mode_32 3
		.amdhsa_float_denorm_mode_16_64 3
		.amdhsa_dx10_clamp 1
		.amdhsa_ieee_mode 1
		.amdhsa_fp16_overflow 0
		.amdhsa_tg_split 0
		.amdhsa_exception_fp_ieee_invalid_op 0
		.amdhsa_exception_fp_denorm_src 0
		.amdhsa_exception_fp_ieee_div_zero 0
		.amdhsa_exception_fp_ieee_overflow 0
		.amdhsa_exception_fp_ieee_underflow 0
		.amdhsa_exception_fp_ieee_inexact 0
		.amdhsa_exception_int_div_zero 0
	.end_amdhsa_kernel

amdhsa.kernels:
  - .agpr_count:     0
    .args:
      - .offset:         0
        .size:           208
        .value_kind:     by_value
      - .offset:         208
        .size:           4
        .value_kind:     hidden_block_count_x
      - .offset:         212
        .size:           4
        .value_kind:     hidden_block_count_y
      - .offset:         216
        .size:           4
        .value_kind:     hidden_block_count_z
      - .offset:         220
        .size:           2
        .value_kind:     hidden_group_size_x
      - .offset:         222
        .size:           2
        .value_kind:     hidden_group_size_y
      - .offset:         224
        .size:           2
        .value_kind:     hidden_group_size_z
      - .offset:         226
        .size:           2
        .value_kind:     hidden_remainder_x
      - .offset:         228
        .size:           2
        .value_kind:     hidden_remainder_y
      - .offset:         230
        .size:           2
        .value_kind:     hidden_remainder_z
      - .offset:         248
        .size:           8
        .value_kind:     hidden_global_offset_x
      - .offset:         256
        .size:           8
        .value_kind:     hidden_global_offset_y
      - .offset:         264
        .size:           8
        .value_kind:     hidden_global_offset_z
      - .offset:         272
        .size:           2
        .value_kind:     hidden_grid_dims
      - .offset:         328
        .size:           4
        .value_kind:     hidden_dynamic_lds_size
    .group_segment_fixed_size: 0
    .kernarg_segment_align: 8
    .kernarg_segment_size: 464
    .language:       OpenCL C
    .language_version:
      - 2
      - 0
    .max_flat_workgroup_size: 512
    .name:           _Z3fwd4Args
    .private_segment_fixed_size: 0
    .sgpr_count:     94
    .sgpr_spill_count: 0
    .symbol:         _Z3fwd4Args.kd
    .uniform_work_group_size: 1
    .uses_dynamic_stack: false
    .vgpr_count:     256
    .vgpr_spill_count: 0
    .wavefront_size: 64
